# indexer count pass: the two packed-u16 accumulation chains interleaved so no s_nop padding is needed (54 instead of 73 instructions per 16-key group)
# baseline (speedup 1.0000x reference)
.LBB0_667:
	v_mov_b32_e32 v8, 0x10001
	s_waitcnt vmcnt(6)
	s_sub_i32 s18, s0, 48
	s_cmp_gt_i32 s18, s81
	v_pk_sub_u16 v9, v188, v5 clamp
	v_xor_b32_e32 v13, v5, v188
	v_pk_sub_u16 v14, v189, v5 clamp
	v_xor_b32_e32 v16, v5, v189
	v_pk_min_u16 v9, v9, v8
	v_pk_min_u16 v13, v13, v8
	v_pk_min_u16 v14, v14, v8
	v_pk_min_u16 v16, v16, v8
	v_pk_add_u16 v9, v9, v14
	v_pk_add_u16 v13, v13, v16
	v_pk_sub_u16 v14, v190, v5 clamp
	v_xor_b32_e32 v16, v5, v190
	v_pk_min_u16 v14, v14, v8
	v_pk_min_u16 v16, v16, v8
	v_pk_add_u16 v9, v9, v14
	v_pk_add_u16 v13, v13, v16
	v_pk_sub_u16 v14, v191, v5 clamp
	v_xor_b32_e32 v16, v5, v191
	v_pk_min_u16 v14, v14, v8
	v_pk_min_u16 v16, v16, v8
	v_pk_add_u16 v9, v9, v14
	v_pk_add_u16 v13, v13, v16
	v_pk_sub_u16 v14, v180, v5 clamp
	v_xor_b32_e32 v16, v5, v180
	v_pk_min_u16 v14, v14, v8
	v_pk_min_u16 v16, v16, v8
	v_pk_add_u16 v9, v9, v14
	v_pk_add_u16 v13, v13, v16
	v_pk_sub_u16 v14, v181, v5 clamp
	v_xor_b32_e32 v16, v5, v181
	v_pk_min_u16 v14, v14, v8
	v_pk_min_u16 v16, v16, v8
	v_pk_add_u16 v9, v9, v14
	v_pk_add_u16 v13, v13, v16
	v_pk_sub_u16 v14, v182, v5 clamp
	v_xor_b32_e32 v16, v5, v182
	v_pk_min_u16 v14, v14, v8
	v_pk_min_u16 v16, v16, v8
	v_pk_add_u16 v9, v9, v14
	v_pk_add_u16 v13, v13, v16
	v_pk_sub_u16 v14, v183, v5 clamp
	v_xor_b32_e32 v16, v5, v183
	v_pk_min_u16 v14, v14, v8
	v_pk_min_u16 v16, v16, v8
	v_pk_add_u16 v9, v9, v14
	v_pk_add_u16 v13, v13, v16
	v_add_u16_sdwa v9, v9, v9 dst_sel:DWORD dst_unused:UNUSED_PAD src0_sel:DWORD src1_sel:WORD_1
	v_add_u16_sdwa v8, v13, v13 dst_sel:BYTE_1 dst_unused:UNUSED_PAD src0_sel:DWORD src1_sel:WORD_1
	s_nop 0
	v_sub_u16_e32 v8, 0x1000, v8
	v_or_b32_e32 v8, v8, v9
	ds_write_b16 v6, v8
	s_cbranch_scc1 .LBB0_673
	v_mov_b32_e32 v8, 0x10001
	s_waitcnt vmcnt(4)
	v_pk_sub_u16 v9, v176, v5 clamp
	v_xor_b32_e32 v13, v5, v176
	v_pk_sub_u16 v14, v177, v5 clamp
	v_xor_b32_e32 v16, v5, v177
	v_pk_min_u16 v9, v9, v8
	v_pk_min_u16 v13, v13, v8
	v_pk_min_u16 v14, v14, v8
	v_pk_min_u16 v16, v16, v8
	v_pk_add_u16 v9, v9, v14
	v_pk_add_u16 v13, v13, v16
	v_pk_sub_u16 v14, v178, v5 clamp
	v_xor_b32_e32 v16, v5, v178
	v_pk_min_u16 v14, v14, v8
	v_pk_min_u16 v16, v16, v8
	v_pk_add_u16 v9, v9, v14
	v_pk_add_u16 v13, v13, v16
	v_pk_sub_u16 v14, v179, v5 clamp
	v_xor_b32_e32 v16, v5, v179
	v_pk_min_u16 v14, v14, v8
	v_pk_min_u16 v16, v16, v8
	v_pk_add_u16 v9, v9, v14
	v_pk_add_u16 v13, v13, v16
	v_pk_sub_u16 v14, v172, v5 clamp
	v_xor_b32_e32 v16, v5, v172
	v_pk_min_u16 v14, v14, v8
	v_pk_min_u16 v16, v16, v8
	v_pk_add_u16 v9, v9, v14
	v_pk_add_u16 v13, v13, v16
	v_pk_sub_u16 v14, v173, v5 clamp
	v_xor_b32_e32 v16, v5, v173
	v_pk_min_u16 v14, v14, v8
	v_pk_min_u16 v16, v16, v8
	v_pk_add_u16 v9, v9, v14
	v_pk_add_u16 v13, v13, v16
	v_pk_sub_u16 v14, v174, v5 clamp
	v_xor_b32_e32 v16, v5, v174
	v_pk_min_u16 v14, v14, v8
	v_pk_min_u16 v16, v16, v8
	v_pk_add_u16 v9, v9, v14
	v_pk_add_u16 v13, v13, v16
	v_pk_sub_u16 v14, v175, v5 clamp
	v_xor_b32_e32 v16, v5, v175
	v_pk_min_u16 v14, v14, v8
	v_pk_min_u16 v16, v16, v8
	v_pk_add_u16 v9, v9, v14
	v_pk_add_u16 v13, v13, v16
	v_add_u16_sdwa v9, v9, v9 dst_sel:DWORD dst_unused:UNUSED_PAD src0_sel:DWORD src1_sel:WORD_1
	v_add_u16_sdwa v8, v13, v13 dst_sel:BYTE_1 dst_unused:UNUSED_PAD src0_sel:DWORD src1_sel:WORD_1
	s_nop 0
	v_sub_u16_e32 v8, 0x1000, v8
	v_or_b32_e32 v8, v8, v9
	ds_write_b16 v6, v8 offset:32
	s_sub_i32 s18, s0, 40
	s_cmp_gt_i32 s18, s81
	s_cbranch_scc0 .LBB0_674

.LBB0_670:
	v_mov_b32_e32 v8, 0x10001
	s_waitcnt vmcnt(0)
	v_pk_sub_u16 v9, v156, v5 clamp
	v_xor_b32_e32 v13, v5, v156
	v_pk_sub_u16 v14, v157, v5 clamp
	v_xor_b32_e32 v16, v5, v157
	v_pk_min_u16 v9, v9, v8
	v_pk_min_u16 v13, v13, v8
	v_pk_min_u16 v14, v14, v8
	v_pk_min_u16 v16, v16, v8
	v_pk_add_u16 v9, v9, v14
	v_pk_add_u16 v13, v13, v16
	v_pk_sub_u16 v14, v158, v5 clamp
	v_xor_b32_e32 v16, v5, v158
	v_pk_min_u16 v14, v14, v8
	v_pk_min_u16 v16, v16, v8
	v_pk_add_u16 v9, v9, v14
	v_pk_add_u16 v13, v13, v16
	v_pk_sub_u16 v14, v159, v5 clamp
	v_xor_b32_e32 v16, v5, v159
	v_pk_min_u16 v14, v14, v8
	v_pk_min_u16 v16, v16, v8
	v_pk_add_u16 v9, v9, v14
	v_pk_add_u16 v13, v13, v16
	v_pk_sub_u16 v14, v152, v5 clamp
	v_xor_b32_e32 v16, v5, v152
	v_pk_min_u16 v14, v14, v8
	v_pk_min_u16 v16, v16, v8
	v_pk_add_u16 v9, v9, v14
	v_pk_add_u16 v13, v13, v16
	v_pk_sub_u16 v14, v153, v5 clamp
	v_xor_b32_e32 v16, v5, v153
	v_pk_min_u16 v14, v14, v8
	v_pk_min_u16 v16, v16, v8
	v_pk_add_u16 v9, v9, v14
	v_pk_add_u16 v13, v13, v16
	v_pk_sub_u16 v14, v154, v5 clamp
	v_xor_b32_e32 v16, v5, v154
	v_pk_min_u16 v14, v14, v8
	v_pk_min_u16 v16, v16, v8
	v_pk_add_u16 v9, v9, v14
	v_pk_add_u16 v13, v13, v16
	v_pk_sub_u16 v14, v155, v5 clamp
	v_xor_b32_e32 v16, v5, v155
	v_pk_min_u16 v14, v14, v8
	v_pk_min_u16 v16, v16, v8
	v_pk_add_u16 v9, v9, v14
	v_pk_add_u16 v13, v13, v16
	v_add_u16_sdwa v9, v9, v9 dst_sel:DWORD dst_unused:UNUSED_PAD src0_sel:DWORD src1_sel:WORD_1
	v_add_u16_sdwa v8, v13, v13 dst_sel:BYTE_1 dst_unused:UNUSED_PAD src0_sel:DWORD src1_sel:WORD_1
	s_nop 0
	v_sub_u16_e32 v8, 0x1000, v8
	v_or_b32_e32 v8, v8, v9
	ds_write_b16 v6, v8 offset:96

.LBB0_674:
	v_mov_b32_e32 v8, 0x10001
	s_waitcnt vmcnt(2)
	v_pk_sub_u16 v9, v164, v5 clamp
	v_xor_b32_e32 v13, v5, v164
	v_pk_sub_u16 v14, v165, v5 clamp
	v_xor_b32_e32 v16, v5, v165
	v_pk_min_u16 v9, v9, v8
	v_pk_min_u16 v13, v13, v8
	v_pk_min_u16 v14, v14, v8
	v_pk_min_u16 v16, v16, v8
	v_pk_add_u16 v9, v9, v14
	v_pk_add_u16 v13, v13, v16
	v_pk_sub_u16 v14, v166, v5 clamp
	v_xor_b32_e32 v16, v5, v166
	v_pk_min_u16 v14, v14, v8
	v_pk_min_u16 v16, v16, v8
	v_pk_add_u16 v9, v9, v14
	v_pk_add_u16 v13, v13, v16
	v_pk_sub_u16 v14, v167, v5 clamp
	v_xor_b32_e32 v16, v5, v167
	v_pk_min_u16 v14, v14, v8
	v_pk_min_u16 v16, v16, v8
	v_pk_add_u16 v9, v9, v14
	v_pk_add_u16 v13, v13, v16
	v_pk_sub_u16 v14, v160, v5 clamp
	v_xor_b32_e32 v16, v5, v160
	v_pk_min_u16 v14, v14, v8
	v_pk_min_u16 v16, v16, v8
	v_pk_add_u16 v9, v9, v14
	v_pk_add_u16 v13, v13, v16
	v_pk_sub_u16 v14, v161, v5 clamp
	v_xor_b32_e32 v16, v5, v161
	v_pk_min_u16 v14, v14, v8
	v_pk_min_u16 v16, v16, v8
	v_pk_add_u16 v9, v9, v14
	v_pk_add_u16 v13, v13, v16
	v_pk_sub_u16 v14, v162, v5 clamp
	v_xor_b32_e32 v16, v5, v162
	v_pk_min_u16 v14, v14, v8
	v_pk_min_u16 v16, v16, v8
	v_pk_add_u16 v9, v9, v14
	v_pk_add_u16 v13, v13, v16
	v_pk_sub_u16 v14, v163, v5 clamp
	v_xor_b32_e32 v16, v5, v163
	v_pk_min_u16 v14, v14, v8
	v_pk_min_u16 v16, v16, v8
	v_pk_add_u16 v9, v9, v14
	v_pk_add_u16 v13, v13, v16
	v_add_u16_sdwa v9, v9, v9 dst_sel:DWORD dst_unused:UNUSED_PAD src0_sel:DWORD src1_sel:WORD_1
	v_add_u16_sdwa v8, v13, v13 dst_sel:BYTE_1 dst_unused:UNUSED_PAD src0_sel:DWORD src1_sel:WORD_1
	s_nop 0
	v_sub_u16_e32 v8, 0x1000, v8
	v_or_b32_e32 v8, v8, v9
	ds_write_b16 v6, v8 offset:64
	s_sub_i32 s18, s0, 32
	s_cmp_gt_i32 s18, s81
	s_cbranch_scc0 .LBB0_670
	s_branch .LBB0_671
